# setup fix + expert-weight conversion keeps next item's loads in flight (counted vmcnt)
# speedup vs baseline: 1.5565x; 1.0090x over previous
; __device__ __forceinline__ ConvDesc expert_desc(Frame& F, int r) {
;     ...
;     if (r < I_G1) { const int e = r >> 10, r2 = r & 1023, kb = r2 >> 5, nb = r2 & 31, pn = nb >> 3, p0 = (nb & 7) * 32;
;         d.src = (p0 < 128) ? (e < NEXP ? INF(I_WEG) + (size_t)e * 2048 * 512 : INF(I_WSG)) + 128 * pn + p0
;                            : (e < NEXP ? INF(I_WEU) + (size_t)e * 2048 * 512 : INF(I_WSU)) + 128 * pn + (p0 - 128);
;         d.ldw = 512; d.k0 = kb * 64; d.dst = WSP(unsigned char, WS_WG1) + ((size_t)e * 1024 + nb * 32) * 2048; d.Kd = 2048; d.sc = pg8::F8_SW1; }
;     else { r -= I_G1; const int e = r >> 9, r2 = r & 511, kb = r2 >> 6, nb = r2 & 63;
;         d.src = (e < NEXP ? INF(I_WED) + (size_t)e * 512 * 2048 : INF(I_WSD)) + nb * 32;
;         d.ldw = 2048; d.k0 = kb * 64; d.dst = WSP(unsigned char, WS_WG2) + ((size_t)e * 2048 + nb * 32) * 512; d.Kd = 512; d.sc = pg8::F8_SW2; }
;     return d;
; }
; __device__ __forceinline__ void conv_load(const ConvDesc& d, float (&v)[32], int lane) {
; #pragma unroll
;     for (int i = 0; i < 32; ++i) { const int kk = 2 * i + (lane >> 5); v[i] = d.src[(size_t)(d.k0 + kk) * d.ldw + (lane & 31)]; }
; }
.LBB0_692:
	s_and_b32 s4, s19, 0x7c0
	v_or_b32_e32 v1, s4, v33
	v_lshlrev_b32_e32 v36, 2, v34
	v_lshl_add_u64 v[2:3], s[24:25], 0, v[36:37]
	v_lshlrev_b32_e32 v36, 11, v1
	v_lshl_add_u64 v[2:3], v[2:3], 0, v[36:37]
	v_add_co_u32_e32 v30, vcc, s36, v2
	s_lshl_b64 s[6:7], s[6:7], 21
	s_nop 0
	v_addc_co_u32_e32 v31, vcc, 0, v3, vcc
	v_add_co_u32_e32 v86, vcc, s37, v2
	s_add_u32 s6, s54, s6
	s_nop 0
	v_addc_co_u32_e32 v87, vcc, 0, v3, vcc
	v_add_co_u32_e32 v6, vcc, s42, v2
	s_addc_u32 s7, s55, s7
	s_nop 0
	v_addc_co_u32_e32 v7, vcc, 0, v3, vcc
	v_add_co_u32_e32 v8, vcc, s43, v2
	s_nop 1
	v_addc_co_u32_e32 v9, vcc, 0, v3, vcc
	v_add_co_u32_e32 v10, vcc, s44, v2
	s_nop 1
	v_addc_co_u32_e32 v11, vcc, 0, v3, vcc
	v_add_co_u32_e32 v12, vcc, s45, v2
	s_nop 1
	v_addc_co_u32_e32 v13, vcc, 0, v3, vcc
	v_add_co_u32_e32 v14, vcc, s46, v2
	s_nop 1
	v_addc_co_u32_e32 v15, vcc, 0, v3, vcc
	v_add_co_u32_e32 v16, vcc, s47, v2
	s_nop 1
	v_addc_co_u32_e32 v17, vcc, 0, v3, vcc
	v_add_co_u32_e32 v18, vcc, s48, v2
	s_nop 1
	v_addc_co_u32_e32 v19, vcc, 0, v3, vcc
	v_add_co_u32_e32 v20, vcc, s49, v2
	s_nop 1
	v_addc_co_u32_e32 v21, vcc, 0, v3, vcc
	v_add_co_u32_e32 v22, vcc, s50, v2
	s_nop 1
	v_addc_co_u32_e32 v23, vcc, 0, v3, vcc
	v_add_co_u32_e32 v24, vcc, s51, v2
	s_nop 1
	v_addc_co_u32_e32 v25, vcc, 0, v3, vcc
	v_add_co_u32_e32 v26, vcc, s52, v2
	s_nop 1
	v_addc_co_u32_e32 v27, vcc, 0, v3, vcc
	v_add_co_u32_e32 v28, vcc, s53, v2
	s_nop 1
	v_addc_co_u32_e32 v29, vcc, 0, v3, vcc
	v_add_co_u32_e32 v88, vcc, 0x1d000, v2
	s_nop 1
	v_addc_co_u32_e32 v89, vcc, 0, v3, vcc
	v_add_co_u32_e32 v90, vcc, 0x1e000, v2
	s_nop 1
	v_addc_co_u32_e32 v91, vcc, 0, v3, vcc
	v_add_co_u32_e32 v92, vcc, 0x1f000, v2
	s_nop 1
	v_addc_co_u32_e32 v93, vcc, 0, v3, vcc
	global_load_dword v5, v[6:7], off offset:-4096
	s_nop 0
	global_load_dword v6, v[6:7], off
	s_nop 0
	global_load_dword v7, v[8:9], off offset:-4096
	s_nop 0
	global_load_dword v8, v[8:9], off
	s_nop 0
	global_load_dword v9, v[10:11], off offset:-4096
	s_nop 0
	global_load_dword v10, v[10:11], off
	s_nop 0
	global_load_dword v11, v[12:13], off offset:-4096
	s_nop 0
	global_load_dword v12, v[12:13], off
	s_nop 0
	global_load_dword v13, v[14:15], off offset:-4096
	s_nop 0
	global_load_dword v14, v[14:15], off
	s_nop 0
	global_load_dword v15, v[16:17], off offset:-4096
	s_nop 0
	global_load_dword v16, v[16:17], off
	s_nop 0
	global_load_dword v17, v[18:19], off offset:-4096
	s_nop 0
	global_load_dword v18, v[18:19], off
	s_nop 0
	global_load_dword v19, v[20:21], off offset:-4096
	s_nop 0
	global_load_dword v20, v[20:21], off
	s_nop 0
	global_load_dword v21, v[22:23], off offset:-4096
	s_nop 0
	global_load_dword v22, v[22:23], off
	s_nop 0
	global_load_dword v23, v[24:25], off offset:-4096
	s_nop 0
	global_load_dword v24, v[24:25], off
	s_nop 0
	global_load_dword v25, v[26:27], off offset:-4096
	s_nop 0
	global_load_dword v26, v[26:27], off
	s_nop 0
	global_load_dword v27, v[28:29], off offset:-4096
	s_nop 0
	global_load_dword v28, v[28:29], off
	s_nop 0
	global_load_dword v2, v[2:3], off
	s_nop 0
	global_load_dword v1, v[30:31], off offset:-4096
	global_load_dword v4, v[30:31], off
	global_load_dword v3, v[86:87], off offset:-4096
	global_load_dword v32, v[86:87], off
	global_load_dword v29, v[88:89], off
	s_nop 0
	global_load_dword v30, v[90:91], off
	global_load_dword v31, v[92:93], off
	s_waitcnt vmcnt(32)
	s_branch .Lmy_cA_s2
.LBB0_693:
	s_waitcnt vmcnt(0)
; #define LAS __attribute__((address_space(3)))
; __device__ __forceinline__ float clamp_f8(float v) { return __builtin_amdgcn_fmed3f(v, -448.f, 448.f); }
; #define LDS_WAIT() asm volatile("s_waitcnt lgkmcnt(0)" ::: "memory")
; __device__ __forceinline__ void conv_store(const ConvDesc& d, const float (&v)[32], LAS float* scr, int lane) {
; #pragma unroll
;     for (int i = 0; i < 32; ++i) { const int kk = 2 * i + (lane >> 5); scr[kk * 33 + (lane & 31)] = pg8::clamp_f8(v[i] * d.sc); }
;     LDS_WAIT(); asm volatile("" ::: "memory");
;     const int n = lane & 31, h = lane >> 5; const LAS float* sp = scr + (32 * h) * 33 + n;
;     u32x4 o0, o1;
; #pragma unroll
;     for (int q = 0; q < 4; ++q) { int w0 = 0, w1 = 0;
;         w0 = __builtin_amdgcn_cvt_pk_fp8_f32(sp[(4 * q + 0) * 33], sp[(4 * q + 1) * 33], w0, false); w0 = __builtin_amdgcn_cvt_pk_fp8_f32(sp[(4 * q + 2) * 33], sp[(4 * q + 3) * 33], w0, true);
;         w1 = __builtin_amdgcn_cvt_pk_fp8_f32(sp[(16 + 4 * q + 0) * 33], sp[(16 + 4 * q + 1) * 33], w1, false); w1 = __builtin_amdgcn_cvt_pk_fp8_f32(sp[(16 + 4 * q + 2) * 33], sp[(16 + 4 * q + 3) * 33], w1, true);
;         o0[q] = (unsigned)w0; o1[q] = (unsigned)w1; }
;     unsigned char* dp = d.dst + (size_t)n * d.Kd + d.k0 + 32 * h;
;     *(u32x4*)dp = o0; *(u32x4*)(dp + 16) = o1;
;     LDS_WAIT(); asm volatile("" ::: "memory");
.Lmy_cA_s2:
	v_mul_f32_e32 v36, 0x42800000, v75
	v_mul_f32_e32 v86, 0x42800000, v74
	v_med3_f32 v36, v36, s57, v35
	v_med3_f32 v86, v86, s57, v35
	ds_write2_b32 v42, v36, v86 offset1:66
	v_mul_f32_e32 v36, 0x42800000, v73
	v_mul_f32_e32 v86, 0x42800000, v72
	v_med3_f32 v36, v36, s57, v35
	v_med3_f32 v86, v86, s57, v35
	ds_write2_b32 v42, v36, v86 offset0:132 offset1:198
	v_mul_f32_e32 v36, 0x42800000, v71
	v_mul_f32_e32 v86, 0x42800000, v49
	v_med3_f32 v36, v36, s57, v35
	v_med3_f32 v86, v86, s57, v35
	ds_write2_b32 v77, v36, v86 offset0:8 offset1:74
	v_mul_f32_e32 v36, 0x42800000, v48
	v_mul_f32_e32 v86, 0x42800000, v47
	v_med3_f32 v36, v36, s57, v35
	v_med3_f32 v86, v86, s57, v35
	ds_write2_b32 v77, v36, v86 offset0:140 offset1:206
	v_mul_f32_e32 v36, 0x42800000, v46
	v_mul_f32_e32 v77, 0x42800000, v45
	v_med3_f32 v36, v36, s57, v35
	v_med3_f32 v77, v77, s57, v35
	ds_write2_b32 v78, v36, v77 offset0:16 offset1:82
	v_mul_f32_e32 v36, 0x42800000, v44
	v_mul_f32_e32 v77, 0x42800000, v51
	v_med3_f32 v36, v36, s57, v35
	v_med3_f32 v77, v77, s57, v35
	ds_write2_b32 v78, v36, v77 offset0:148 offset1:214
	v_mul_f32_e32 v36, 0x42800000, v50
	v_mul_f32_e32 v77, 0x42800000, v57
	v_med3_f32 v36, v36, s57, v35
	v_med3_f32 v77, v77, s57, v35
	ds_write2_b32 v79, v36, v77 offset0:24 offset1:90
	v_mul_f32_e32 v36, 0x42800000, v56
	v_mul_f32_e32 v77, 0x42800000, v55
	v_med3_f32 v36, v36, s57, v35
	v_med3_f32 v77, v77, s57, v35
	ds_write2_b32 v79, v36, v77 offset0:156 offset1:222
	v_mul_f32_e32 v36, 0x42800000, v54
	v_mul_f32_e32 v77, 0x42800000, v53
	v_med3_f32 v36, v36, s57, v35
	v_med3_f32 v77, v77, s57, v35
	ds_write2_b32 v80, v36, v77 offset0:32 offset1:98
	v_mul_f32_e32 v36, 0x42800000, v52
	v_mul_f32_e32 v77, 0x42800000, v59
	v_med3_f32 v36, v36, s57, v35
	v_med3_f32 v77, v77, s57, v35
	ds_write2_b32 v80, v36, v77 offset0:164 offset1:230
	v_mul_f32_e32 v36, 0x42800000, v58
	v_mul_f32_e32 v77, 0x42800000, v65
	v_med3_f32 v36, v36, s57, v35
	v_med3_f32 v77, v77, s57, v35
	ds_write2_b32 v81, v36, v77 offset0:40 offset1:106
	v_mul_f32_e32 v36, 0x42800000, v64
	v_mul_f32_e32 v77, 0x42800000, v63
	v_med3_f32 v36, v36, s57, v35
	v_med3_f32 v77, v77, s57, v35
	ds_write2_b32 v81, v36, v77 offset0:172 offset1:238
	v_mul_f32_e32 v36, 0x42800000, v62
	v_mul_f32_e32 v77, 0x42800000, v61
	v_med3_f32 v36, v36, s57, v35
	v_med3_f32 v77, v77, s57, v35
	ds_write2_b32 v82, v36, v77 offset0:48 offset1:114
	v_mul_f32_e32 v36, 0x42800000, v60
	v_mul_f32_e32 v77, 0x42800000, v67
	v_med3_f32 v36, v36, s57, v35
	v_med3_f32 v77, v77, s57, v35
	ds_write2_b32 v82, v36, v77 offset0:180 offset1:246
	v_mul_f32_e32 v36, 0x42800000, v66
	v_mul_f32_e32 v77, 0x42800000, v69
	v_med3_f32 v36, v36, s57, v35
	v_med3_f32 v77, v77, s57, v35
	ds_write2_b32 v83, v36, v77 offset0:56 offset1:122
	v_mul_f32_e32 v36, 0x42800000, v68
	v_mul_f32_e32 v77, 0x42800000, v70
	v_med3_f32 v36, v36, s57, v35
	v_med3_f32 v77, v77, s57, v35
	ds_write2_b32 v83, v36, v77 offset0:188 offset1:254
	s_waitcnt lgkmcnt(0)
	ds_read2_b32 v[80:81], v43 offset1:33
	v_mov_b32_e32 v78, v37
	ds_read2_b32 v[82:83], v43 offset0:66 offset1:99
	v_mov_b32_e32 v79, v37
	ds_read2_b32 v[88:89], v85 offset0:148 offset1:181
	s_waitcnt lgkmcnt(2)
	v_cvt_pk_fp8_f32 v78, v80, v81
	ds_read2_b32 v[80:81], v85 offset0:16 offset1:49
	v_mov_b32_e32 v86, v37
	v_mov_b32_e32 v87, v37
	s_waitcnt lgkmcnt(2)
	v_cvt_pk_fp8_f32 v78, v82, v83 op_sel:[0,0,1]
	ds_read2_b32 v[82:83], v43 offset0:132 offset1:165
	s_waitcnt lgkmcnt(1)
	v_cvt_pk_fp8_f32 v86, v80, v81
	ds_read2_b32 v[80:81], v85 offset0:82 offset1:115
	ds_read2_b32 v[90:91], v85 offset0:214 offset1:247
	v_cvt_pk_fp8_f32 v87, v88, v89
	s_waitcnt lgkmcnt(2)
	v_cvt_pk_fp8_f32 v79, v82, v83
	ds_read2_b32 v[82:83], v43 offset0:198 offset1:231
	ds_read2_b32 v[88:89], v76 offset0:8 offset1:41
	ds_read2_b32 v[92:93], v76 offset0:140 offset1:173
	ds_read2_b32 v[94:95], v84 offset0:156 offset1:189
	s_waitcnt lgkmcnt(5)
	v_cvt_pk_fp8_f32 v86, v80, v81 op_sel:[0,0,1]
	s_waitcnt lgkmcnt(3)
	v_cvt_pk_fp8_f32 v79, v82, v83 op_sel:[0,0,1]
	ds_read2_b32 v[82:83], v84 offset0:24 offset1:57
	v_mov_b32_e32 v80, v37
	v_cvt_pk_fp8_f32 v87, v90, v91 op_sel:[0,0,1]
	s_waitcnt lgkmcnt(3)
	v_cvt_pk_fp8_f32 v80, v88, v89
	ds_read2_b32 v[90:91], v76 offset0:74 offset1:107
	v_mov_b32_e32 v88, v37
	v_mov_b32_e32 v81, v37
	ds_read2_b32 v[76:77], v76 offset0:206 offset1:239
	s_waitcnt lgkmcnt(2)
	v_cvt_pk_fp8_f32 v88, v82, v83
	ds_read2_b32 v[82:83], v84 offset0:90 offset1:123
	v_cvt_pk_fp8_f32 v81, v92, v93
	v_mov_b32_e32 v89, v37
	ds_read2_b32 v[84:85], v84 offset0:222 offset1:255
	v_cvt_pk_fp8_f32 v89, v94, v95
	s_waitcnt lgkmcnt(3)
	v_cvt_pk_fp8_f32 v80, v90, v91 op_sel:[0,0,1]
	s_waitcnt lgkmcnt(2)
	v_cvt_pk_fp8_f32 v81, v76, v77 op_sel:[0,0,1]
	s_waitcnt lgkmcnt(1)
	v_cvt_pk_fp8_f32 v88, v82, v83 op_sel:[0,0,1]
	s_waitcnt lgkmcnt(0)
	v_cvt_pk_fp8_f32 v89, v84, v85 op_sel:[0,0,1]
	v_lshl_add_u64 v[76:77], s[10:11], 0, v[40:41]
	s_mov_b32 s9, s5
	v_lshl_add_u64 v[76:77], v[76:77], 0, s[8:9]
	v_lshl_add_u64 v[76:77], v[76:77], 0, v[38:39]
	global_store_dwordx4 v[76:77], v[78:81], off
	global_store_dwordx4 v[76:77], v[86:89], off offset:16
	s_waitcnt lgkmcnt(0)
	s_add_i32 s56, s56, 0x10000
	s_addk_i32 s19, 0x1000

; __device__ __forceinline__ ConvDesc expert_desc(Frame& F, int r) {
;     ...
;     if (r < I_G1) { const int e = r >> 10, r2 = r & 1023, kb = r2 >> 5, nb = r2 & 31, pn = nb >> 3, p0 = (nb & 7) * 32;
;         d.src = (p0 < 128) ? (e < NEXP ? INF(I_WEG) + (size_t)e * 2048 * 512 : INF(I_WSG)) + 128 * pn + p0
;                            : (e < NEXP ? INF(I_WEU) + (size_t)e * 2048 * 512 : INF(I_WSU)) + 128 * pn + (p0 - 128);
;         d.ldw = 512; d.k0 = kb * 64; d.dst = WSP(unsigned char, WS_WG1) + ((size_t)e * 1024 + nb * 32) * 2048; d.Kd = 2048; d.sc = pg8::F8_SW1; }
;     else { r -= I_G1; const int e = r >> 9, r2 = r & 511, kb = r2 >> 6, nb = r2 & 63;
;         d.src = (e < NEXP ? INF(I_WED) + (size_t)e * 512 * 2048 : INF(I_WSD)) + nb * 32;
;         d.ldw = 2048; d.k0 = kb * 64; d.dst = WSP(unsigned char, WS_WG2) + ((size_t)e * 2048 + nb * 32) * 512; d.Kd = 512; d.sc = pg8::F8_SW2; }
;     return d;
; }
; __device__ __forceinline__ void conv_load(const ConvDesc& d, float (&v)[32], int lane) {
; #pragma unroll
;     for (int i = 0; i < 32; ++i) { const int kk = 2 * i + (lane >> 5); v[i] = d.src[(size_t)(d.k0 + kk) * d.ldw + (lane & 31)]; }
; }
.LBB0_700:
	s_and_b32 s8, s19, 0x7c0
	v_or_b32_e32 v46, s8, v33
	v_lshlrev_b32_e32 v36, 2, v34
	v_lshl_add_u64 v[44:45], s[24:25], 0, v[36:37]
	v_lshlrev_b32_e32 v36, 11, v46
	v_lshl_add_u64 v[68:69], v[44:45], 0, v[36:37]
	v_add_co_u32_e32 v70, vcc, s36, v68
	s_lshl_b64 s[10:11], s[10:11], 21
	s_nop 0
	v_addc_co_u32_e32 v71, vcc, 0, v69, vcc
	v_add_co_u32_e32 v76, vcc, s37, v68
	s_add_u32 s10, s54, s10
	s_nop 0
	v_addc_co_u32_e32 v77, vcc, 0, v69, vcc
	v_add_co_u32_e32 v44, vcc, s42, v68
	s_addc_u32 s11, s55, s11
	s_nop 0
	v_addc_co_u32_e32 v45, vcc, 0, v69, vcc
	v_add_co_u32_e32 v50, vcc, s43, v68
	s_nop 1
	v_addc_co_u32_e32 v51, vcc, 0, v69, vcc
	v_add_co_u32_e32 v52, vcc, s44, v68
	s_nop 1
	v_addc_co_u32_e32 v53, vcc, 0, v69, vcc
	v_add_co_u32_e32 v54, vcc, s45, v68
	s_nop 1
	v_addc_co_u32_e32 v55, vcc, 0, v69, vcc
	global_load_dword v49, v[44:45], off offset:-4096
	global_load_dword v48, v[44:45], off
	global_load_dword v47, v[50:51], off offset:-4096
	global_load_dword v46, v[50:51], off
	s_nop 0
	global_load_dword v45, v[52:53], off offset:-4096
	global_load_dword v44, v[52:53], off
	global_load_dword v51, v[54:55], off offset:-4096
	global_load_dword v50, v[54:55], off
	v_add_co_u32_e32 v52, vcc, s46, v68
	s_nop 1
	v_addc_co_u32_e32 v53, vcc, 0, v69, vcc
	v_add_co_u32_e32 v58, vcc, s47, v68
	s_nop 1
	v_addc_co_u32_e32 v59, vcc, 0, v69, vcc
	v_add_co_u32_e32 v60, vcc, s48, v68
	s_nop 1
	v_addc_co_u32_e32 v61, vcc, 0, v69, vcc
	v_add_co_u32_e32 v62, vcc, s49, v68
	s_nop 1
	v_addc_co_u32_e32 v63, vcc, 0, v69, vcc
	global_load_dword v57, v[52:53], off offset:-4096
	global_load_dword v56, v[52:53], off
	global_load_dword v55, v[58:59], off offset:-4096
	global_load_dword v54, v[58:59], off
	s_nop 0
	global_load_dword v53, v[60:61], off offset:-4096
	global_load_dword v52, v[60:61], off
	global_load_dword v59, v[62:63], off offset:-4096
	global_load_dword v58, v[62:63], off
	v_add_co_u32_e32 v60, vcc, s50, v68
	s_nop 1
	v_addc_co_u32_e32 v61, vcc, 0, v69, vcc
	v_add_co_u32_e32 v66, vcc, s51, v68
	s_nop 1
	v_addc_co_u32_e32 v67, vcc, 0, v69, vcc
	v_add_co_u32_e32 v72, vcc, s52, v68
	s_nop 1
	v_addc_co_u32_e32 v73, vcc, 0, v69, vcc
	v_add_co_u32_e32 v74, vcc, s53, v68
	s_nop 1
	v_addc_co_u32_e32 v75, vcc, 0, v69, vcc
	v_add_co_u32_e32 v78, vcc, 0x1d000, v68
	global_load_dword v65, v[60:61], off offset:-4096
	global_load_dword v64, v[60:61], off
	global_load_dword v63, v[66:67], off offset:-4096
	global_load_dword v62, v[66:67], off
	s_nop 0
	global_load_dword v61, v[72:73], off offset:-4096
	global_load_dword v60, v[72:73], off
	global_load_dword v67, v[74:75], off offset:-4096
	global_load_dword v66, v[74:75], off
	v_addc_co_u32_e32 v79, vcc, 0, v69, vcc
	v_add_co_u32_e32 v80, vcc, 0x1e000, v68
	s_nop 1
	v_addc_co_u32_e32 v81, vcc, 0, v69, vcc
	v_add_co_u32_e32 v82, vcc, 0x1f000, v68
	s_nop 1
	v_addc_co_u32_e32 v83, vcc, 0, v69, vcc
	global_load_dword v75, v[68:69], off
	global_load_dword v74, v[70:71], off offset:-4096
	global_load_dword v73, v[70:71], off
	global_load_dword v72, v[76:77], off offset:-4096
	s_nop 0
	global_load_dword v71, v[76:77], off
	global_load_dword v69, v[78:79], off
	global_load_dword v68, v[80:81], off
	global_load_dword v70, v[82:83], off
	s_waitcnt vmcnt(32)
	s_branch .Lmy_cA_s1

; #define LAS __attribute__((address_space(3)))
; __device__ __forceinline__ float clamp_f8(float v) { return __builtin_amdgcn_fmed3f(v, -448.f, 448.f); }
; #define LDS_WAIT() asm volatile("s_waitcnt lgkmcnt(0)" ::: "memory")
; __device__ __forceinline__ void conv_store(const ConvDesc& d, const float (&v)[32], LAS float* scr, int lane) {
; #pragma unroll
;     for (int i = 0; i < 32; ++i) { const int kk = 2 * i + (lane >> 5); scr[kk * 33 + (lane & 31)] = pg8::clamp_f8(v[i] * d.sc); }
;     LDS_WAIT(); asm volatile("" ::: "memory");
;     const int n = lane & 31, h = lane >> 5; const LAS float* sp = scr + (32 * h) * 33 + n;
;     u32x4 o0, o1;
; #pragma unroll
;     for (int q = 0; q < 4; ++q) { int w0 = 0, w1 = 0;
;         w0 = __builtin_amdgcn_cvt_pk_fp8_f32(sp[(4 * q + 0) * 33], sp[(4 * q + 1) * 33], w0, false); w0 = __builtin_amdgcn_cvt_pk_fp8_f32(sp[(4 * q + 2) * 33], sp[(4 * q + 3) * 33], w0, true);
;         w1 = __builtin_amdgcn_cvt_pk_fp8_f32(sp[(16 + 4 * q + 0) * 33], sp[(16 + 4 * q + 1) * 33], w1, false); w1 = __builtin_amdgcn_cvt_pk_fp8_f32(sp[(16 + 4 * q + 2) * 33], sp[(16 + 4 * q + 3) * 33], w1, true);
;         o0[q] = (unsigned)w0; o1[q] = (unsigned)w1; }
;     unsigned char* dp = d.dst + (size_t)n * d.Kd + d.k0 + 32 * h;
;     *(u32x4*)dp = o0; *(u32x4*)(dp + 16) = o1;
;     LDS_WAIT(); asm volatile("" ::: "memory");
; }
; __device__ __forceinline__ void convert_expert_range(Frame& F, int first, int end, int stride, LAS float* scr) {
;     if (first >= end) return;
;     const int lane = F.lane;
;     float va[32], vb[32];
;     ConvDesc da = expert_desc(F, first), db = da; conv_load(da, va, lane);
;     for (int it = first; ; it += 2 * stride) {
;         const bool h1 = it + stride < end; if (h1) { db = expert_desc(F, it + stride); conv_load(db, vb, lane); }
;         conv_store(da, va, scr, lane);
;         if (!h1) break;
;         const bool h2 = it + 2 * stride < end; if (h2) { da = expert_desc(F, it + 2 * stride); conv_load(da, va, lane); }
;         conv_store(db, vb, scr, lane);
;         if (!h2) break;
;     }
; }
.Lmy_cA_s1:
	v_mul_f32_e32 v36, 0x42800000, v2
	v_mul_f32_e32 v76, 0x42800000, v1
	v_med3_f32 v36, v36, s57, v35
	v_med3_f32 v76, v76, s57, v35
	ds_write2_b32 v42, v36, v76 offset1:66
	v_mul_f32_e32 v36, 0x42800000, v4
	v_mul_f32_e32 v76, 0x42800000, v3
	v_med3_f32 v36, v36, s57, v35
	v_med3_f32 v76, v76, s57, v35
	ds_write2_b32 v42, v36, v76 offset0:132 offset1:198
	v_mul_f32_e32 v36, 0x42800000, v32
	v_mul_f32_e32 v76, 0x42800000, v5
	v_med3_f32 v36, v36, s57, v35
	v_med3_f32 v76, v76, s57, v35
	v_add_u32_e32 v77, 0x400, v42
	ds_write2_b32 v77, v36, v76 offset0:8 offset1:74
	v_mul_f32_e32 v36, 0x42800000, v6
	v_mul_f32_e32 v76, 0x42800000, v7
	v_med3_f32 v36, v36, s57, v35
	v_med3_f32 v76, v76, s57, v35
	ds_write2_b32 v77, v36, v76 offset0:140 offset1:206
	v_mul_f32_e32 v36, 0x42800000, v8
	v_mul_f32_e32 v76, 0x42800000, v9
	v_med3_f32 v36, v36, s57, v35
	v_med3_f32 v76, v76, s57, v35
	v_add_u32_e32 v78, 0x800, v42
	ds_write2_b32 v78, v36, v76 offset0:16 offset1:82
	v_mul_f32_e32 v36, 0x42800000, v10
	v_mul_f32_e32 v76, 0x42800000, v11
	v_med3_f32 v36, v36, s57, v35
	v_med3_f32 v76, v76, s57, v35
	ds_write2_b32 v78, v36, v76 offset0:148 offset1:214
	v_mul_f32_e32 v36, 0x42800000, v12
	v_mul_f32_e32 v76, 0x42800000, v13
	v_med3_f32 v36, v36, s57, v35
	v_med3_f32 v76, v76, s57, v35
	v_add_u32_e32 v79, 0xc00, v42
	ds_write2_b32 v79, v36, v76 offset0:24 offset1:90
	v_mul_f32_e32 v36, 0x42800000, v14
	v_mul_f32_e32 v76, 0x42800000, v15
	v_med3_f32 v36, v36, s57, v35
	v_med3_f32 v76, v76, s57, v35
	ds_write2_b32 v79, v36, v76 offset0:156 offset1:222
	v_mul_f32_e32 v36, 0x42800000, v16
	v_mul_f32_e32 v76, 0x42800000, v17
	v_med3_f32 v36, v36, s57, v35
	v_med3_f32 v76, v76, s57, v35
	v_add_u32_e32 v80, 0x1000, v42
	ds_write2_b32 v80, v36, v76 offset0:32 offset1:98
	v_mul_f32_e32 v36, 0x42800000, v18
	v_mul_f32_e32 v76, 0x42800000, v19
	v_med3_f32 v36, v36, s57, v35
	v_med3_f32 v76, v76, s57, v35
	ds_write2_b32 v80, v36, v76 offset0:164 offset1:230
	v_mul_f32_e32 v36, 0x42800000, v20
	v_mul_f32_e32 v76, 0x42800000, v21
	v_med3_f32 v36, v36, s57, v35
	v_med3_f32 v76, v76, s57, v35
	v_add_u32_e32 v81, 0x1400, v42
	ds_write2_b32 v81, v36, v76 offset0:40 offset1:106
	v_mul_f32_e32 v36, 0x42800000, v22
	v_mul_f32_e32 v76, 0x42800000, v23
	v_med3_f32 v36, v36, s57, v35
	v_med3_f32 v76, v76, s57, v35
	ds_write2_b32 v81, v36, v76 offset0:172 offset1:238
	v_mul_f32_e32 v36, 0x42800000, v24
	v_mul_f32_e32 v76, 0x42800000, v25
	v_med3_f32 v36, v36, s57, v35
	v_med3_f32 v76, v76, s57, v35
	v_add_u32_e32 v82, 0x1800, v42
	ds_write2_b32 v82, v36, v76 offset0:48 offset1:114
	v_mul_f32_e32 v36, 0x42800000, v26
	v_mul_f32_e32 v76, 0x42800000, v27
	v_med3_f32 v36, v36, s57, v35
	v_med3_f32 v76, v76, s57, v35
	ds_write2_b32 v82, v36, v76 offset0:180 offset1:246
	v_mul_f32_e32 v36, 0x42800000, v28
	v_mul_f32_e32 v76, 0x42800000, v29
	v_med3_f32 v36, v36, s57, v35
	v_med3_f32 v76, v76, s57, v35
	v_add_u32_e32 v83, 0x1c00, v42
	ds_write2_b32 v83, v36, v76 offset0:56 offset1:122
	v_mul_f32_e32 v36, 0x42800000, v30
	v_mul_f32_e32 v76, 0x42800000, v31
	v_med3_f32 v36, v36, s57, v35
	v_med3_f32 v76, v76, s57, v35
	ds_write2_b32 v83, v36, v76 offset0:188 offset1:254
	s_waitcnt lgkmcnt(0)
	ds_read2_b32 v[86:87], v43 offset1:33
	v_mov_b32_e32 v84, v37
	v_mov_b32_e32 v85, v37
	v_add_u32_e32 v76, 0x400, v43
	ds_read2_b32 v[88:89], v76 offset0:8 offset1:41
	s_waitcnt lgkmcnt(1)
	v_cvt_pk_fp8_f32 v84, v86, v87
	ds_read2_b32 v[86:87], v43 offset0:66 offset1:99
	s_andn2_b64 vcc, exec, s[22:23]
	s_mov_b64 s[22:23], -1
	s_waitcnt lgkmcnt(0)
	v_cvt_pk_fp8_f32 v84, v86, v87 op_sel:[0,0,1]
	ds_read2_b32 v[86:87], v43 offset0:132 offset1:165
	s_waitcnt lgkmcnt(0)
	v_cvt_pk_fp8_f32 v85, v86, v87
	ds_read2_b32 v[86:87], v43 offset0:198 offset1:231
	s_waitcnt lgkmcnt(0)
	v_cvt_pk_fp8_f32 v85, v86, v87 op_sel:[0,0,1]
	v_mov_b32_e32 v86, v37
	v_cvt_pk_fp8_f32 v86, v88, v89
	ds_read2_b32 v[88:89], v76 offset0:74 offset1:107
	v_mov_b32_e32 v87, v37
	s_waitcnt lgkmcnt(0)
	v_cvt_pk_fp8_f32 v86, v88, v89 op_sel:[0,0,1]
	ds_read2_b32 v[88:89], v76 offset0:140 offset1:173
	s_waitcnt lgkmcnt(0)
	v_cvt_pk_fp8_f32 v87, v88, v89
	ds_read2_b32 v[88:89], v76 offset0:206 offset1:239
	s_waitcnt lgkmcnt(0)
	v_cvt_pk_fp8_f32 v87, v88, v89 op_sel:[0,0,1]
	v_lshl_add_u64 v[88:89], s[6:7], 0, v[40:41]
	v_lshl_add_u64 v[88:89], v[88:89], 0, s[4:5]
	v_lshl_add_u64 v[90:91], v[88:89], 0, v[38:39]
	global_store_dwordx4 v[90:91], v[84:87], off
	s_nop 1
	v_add_u32_e32 v85, 0x800, v43
	ds_read2_b32 v[88:89], v85 offset0:16 offset1:49
	v_mov_b32_e32 v86, v37
	v_mov_b32_e32 v87, v37
	v_add_u32_e32 v84, 0xc00, v43
	ds_read2_b32 v[92:93], v84 offset0:24 offset1:57
	s_waitcnt lgkmcnt(1)
	v_cvt_pk_fp8_f32 v86, v88, v89
	ds_read2_b32 v[88:89], v85 offset0:82 offset1:115
	s_waitcnt lgkmcnt(0)
	v_cvt_pk_fp8_f32 v86, v88, v89 op_sel:[0,0,1]
	ds_read2_b32 v[88:89], v85 offset0:148 offset1:181
	s_waitcnt lgkmcnt(0)
	v_cvt_pk_fp8_f32 v87, v88, v89
	ds_read2_b32 v[88:89], v85 offset0:214 offset1:247
	s_waitcnt lgkmcnt(0)
	v_cvt_pk_fp8_f32 v87, v88, v89 op_sel:[0,0,1]
	v_mov_b32_e32 v88, v37
	v_cvt_pk_fp8_f32 v88, v92, v93
	ds_read2_b32 v[92:93], v84 offset0:90 offset1:123
	v_mov_b32_e32 v89, v37
	s_waitcnt lgkmcnt(0)
	v_cvt_pk_fp8_f32 v88, v92, v93 op_sel:[0,0,1]
	ds_read2_b32 v[92:93], v84 offset0:156 offset1:189
	s_waitcnt lgkmcnt(0)
	v_cvt_pk_fp8_f32 v89, v92, v93
	ds_read2_b32 v[92:93], v84 offset0:222 offset1:255
	s_waitcnt lgkmcnt(0)
	v_cvt_pk_fp8_f32 v89, v92, v93 op_sel:[0,0,1]
	global_store_dwordx4 v[90:91], v[86:89], off offset:16
	s_waitcnt lgkmcnt(0)
	s_cbranch_vccnz .LBB0_694
	s_add_i32 s58, s40, 0x800
	s_cmp_gt_i32 s40, 0xbaff
	s_cselect_b64 s[22:23], -1, 0
	s_and_b64 vcc, exec, s[22:23]
	s_cbranch_vccnz .LBB0_693
	s_ashr_i32 s6, s58, 10
	s_ashr_i32 s7, s6, 31
	s_and_b32 s4, s56, 0xe0
	s_lshl_b64 s[38:39], s[6:7], 22
	s_cmpk_gt_u32 s4, 0x7f
	s_mov_b64 s[40:41], -1
	s_cbranch_scc0 .LBB0_705
	s_load_dwordx2 s[24:25], s[16:17], 0x90
	s_mov_b64 s[40:41], 0
	s_waitcnt lgkmcnt(0)
	s_add_u32 s9, s24, s38
	s_addc_u32 s24, s25, s39
	s_lshl_b32 s25, s18, 2
	s_add_u32 s9, s9, s25
	s_addc_u32 s24, s24, 0
	s_lshl_b32 s25, s4, 2
	s_add_u32 s9, s9, s25
	s_addc_u32 s25, s24, 0
	s_add_u32 s24, s9, 0xfffffe00
	s_addc_u32 s25, s25, -1

; __device__ __forceinline__ ConvDesc expert_desc(Frame& F, int r) {
;     ...
;     else { r -= I_G1; const int e = r >> 9, r2 = r & 511, kb = r2 >> 6, nb = r2 & 63;
;         d.src = (e < NEXP ? INF(I_WED) + (size_t)e * 512 * 2048 : INF(I_WSD)) + nb * 32;
;         d.ldw = 2048; d.k0 = kb * 64; d.dst = WSP(unsigned char, WS_WG2) + ((size_t)e * 2048 + nb * 32) * 512; d.Kd = 512; d.sc = pg8::F8_SW2; }
;     return d;
; }
; __device__ __forceinline__ void conv_load(const ConvDesc& d, float (&v)[32], int lane) {
; #pragma unroll
;     for (int i = 0; i < 32; ++i) { const int kk = 2 * i + (lane >> 5); v[i] = d.src[(size_t)(d.k0 + kk) * d.ldw + (lane & 31)]; }
; }
.LBB0_968:
	v_or_b32_e32 v1, s6, v35
	v_lshlrev_b32_e32 v36, 2, v34
	v_lshl_add_u64 v[2:3], s[24:25], 0, v[36:37]
	v_mul_hi_u32_u24_e32 v5, s22, v1
	v_mul_u32_u24_e32 v4, s22, v1
	v_lshl_add_u64 v[16:17], v[4:5], 2, v[2:3]
	v_or_b32_e32 v4, 2, v1
	v_mul_hi_u32_u24_e32 v5, s22, v4
	v_mul_u32_u24_e32 v4, s22, v4
	v_lshl_add_u64 v[18:19], v[4:5], 2, v[2:3]
	v_or_b32_e32 v4, 4, v1
	v_mul_hi_u32_u24_e32 v5, s22, v4
	v_mul_u32_u24_e32 v4, s22, v4
	v_lshl_add_u64 v[20:21], v[4:5], 2, v[2:3]
	v_or_b32_e32 v4, 6, v1
	v_mul_hi_u32_u24_e32 v5, s22, v4
	v_mul_u32_u24_e32 v4, s22, v4
	v_lshl_add_u64 v[22:23], v[4:5], 2, v[2:3]
	v_or_b32_e32 v4, 8, v1
	v_mul_hi_u32_u24_e32 v5, s22, v4
	v_mul_u32_u24_e32 v4, s22, v4
	v_lshl_add_u64 v[24:25], v[4:5], 2, v[2:3]
	v_or_b32_e32 v4, 10, v1
	v_mul_hi_u32_u24_e32 v5, s22, v4
	v_mul_u32_u24_e32 v4, s22, v4
	v_lshl_add_u64 v[26:27], v[4:5], 2, v[2:3]
	v_or_b32_e32 v4, 12, v1
	v_mul_hi_u32_u24_e32 v5, s22, v4
	v_mul_u32_u24_e32 v4, s22, v4
	v_lshl_add_u64 v[28:29], v[4:5], 2, v[2:3]
	v_or_b32_e32 v4, 14, v1
	v_mul_hi_u32_u24_e32 v5, s22, v4
	v_mul_u32_u24_e32 v4, s22, v4
	v_lshl_add_u64 v[30:31], v[4:5], 2, v[2:3]
	v_or_b32_e32 v4, 16, v1
	v_mul_hi_u32_u24_e32 v5, s22, v4
	v_mul_u32_u24_e32 v4, s22, v4
	v_lshl_add_u64 v[50:51], v[4:5], 2, v[2:3]
	v_or_b32_e32 v4, 18, v1
	v_mul_hi_u32_u24_e32 v5, s22, v4
	v_mul_u32_u24_e32 v4, s22, v4
	v_lshl_add_u64 v[52:53], v[4:5], 2, v[2:3]
	v_or_b32_e32 v4, 20, v1
	v_mul_hi_u32_u24_e32 v5, s22, v4
	v_mul_u32_u24_e32 v4, s22, v4
	v_lshl_add_u64 v[54:55], v[4:5], 2, v[2:3]
	v_or_b32_e32 v4, 22, v1
	v_mul_hi_u32_u24_e32 v5, s22, v4
	v_mul_u32_u24_e32 v4, s22, v4
	v_lshl_add_u64 v[56:57], v[4:5], 2, v[2:3]
	v_or_b32_e32 v4, 24, v1
	v_mul_hi_u32_u24_e32 v5, s22, v4
	v_mul_u32_u24_e32 v4, s22, v4
	v_lshl_add_u64 v[58:59], v[4:5], 2, v[2:3]
	v_or_b32_e32 v4, 26, v1
	v_mul_hi_u32_u24_e32 v5, s22, v4
	v_mul_u32_u24_e32 v4, s22, v4
	v_lshl_add_u64 v[96:97], v[4:5], 2, v[2:3]
	v_or_b32_e32 v4, 28, v1
	v_mul_hi_u32_u24_e32 v5, s22, v4
	v_mul_u32_u24_e32 v4, s22, v4
	v_lshl_add_u64 v[98:99], v[4:5], 2, v[2:3]
	v_or_b32_e32 v4, 30, v1
	v_mul_hi_u32_u24_e32 v5, s22, v4
	v_mul_u32_u24_e32 v4, s22, v4
	v_lshl_add_u64 v[100:101], v[4:5], 2, v[2:3]
	v_or_b32_e32 v4, 32, v1
	v_mul_hi_u32_u24_e32 v5, s22, v4
	v_mul_u32_u24_e32 v4, s22, v4
	v_lshl_add_u64 v[102:103], v[4:5], 2, v[2:3]
	v_or_b32_e32 v4, 34, v1
	v_mul_hi_u32_u24_e32 v5, s22, v4
	v_mul_u32_u24_e32 v4, s22, v4
	v_lshl_add_u64 v[104:105], v[4:5], 2, v[2:3]
	v_or_b32_e32 v4, 36, v1
	v_mul_hi_u32_u24_e32 v5, s22, v4
	v_mul_u32_u24_e32 v4, s22, v4
	v_lshl_add_u64 v[106:107], v[4:5], 2, v[2:3]
	v_or_b32_e32 v4, 38, v1
	v_mul_hi_u32_u24_e32 v5, s22, v4
	v_mul_u32_u24_e32 v4, s22, v4
	v_lshl_add_u64 v[108:109], v[4:5], 2, v[2:3]
	v_or_b32_e32 v4, 40, v1
	v_mul_hi_u32_u24_e32 v5, s22, v4
	v_mul_u32_u24_e32 v4, s22, v4
	v_lshl_add_u64 v[110:111], v[4:5], 2, v[2:3]
	v_or_b32_e32 v4, 42, v1
	v_mul_hi_u32_u24_e32 v5, s22, v4
	v_mul_u32_u24_e32 v4, s22, v4
	v_lshl_add_u64 v[112:113], v[4:5], 2, v[2:3]
	v_or_b32_e32 v4, 44, v1
	v_mul_hi_u32_u24_e32 v5, s22, v4
	v_mul_u32_u24_e32 v4, s22, v4
	v_lshl_add_u64 v[114:115], v[4:5], 2, v[2:3]
	v_or_b32_e32 v4, 46, v1
	v_mul_hi_u32_u24_e32 v5, s22, v4
	v_mul_u32_u24_e32 v4, s22, v4
	v_lshl_add_u64 v[116:117], v[4:5], 2, v[2:3]
	v_or_b32_e32 v4, 48, v1
	v_mul_hi_u32_u24_e32 v5, s22, v4
	v_mul_u32_u24_e32 v4, s22, v4
	v_lshl_add_u64 v[118:119], v[4:5], 2, v[2:3]
	v_or_b32_e32 v4, 50, v1
	v_mul_hi_u32_u24_e32 v5, s22, v4
	v_mul_u32_u24_e32 v4, s22, v4
	v_lshl_add_u64 v[120:121], v[4:5], 2, v[2:3]
	v_or_b32_e32 v4, 52, v1
	v_mul_hi_u32_u24_e32 v5, s22, v4
	v_mul_u32_u24_e32 v4, s22, v4
	v_lshl_add_u64 v[122:123], v[4:5], 2, v[2:3]
	v_or_b32_e32 v4, 54, v1
	v_mul_hi_u32_u24_e32 v5, s22, v4
	v_mul_u32_u24_e32 v4, s22, v4
	v_lshl_add_u64 v[124:125], v[4:5], 2, v[2:3]
	v_or_b32_e32 v4, 56, v1
	v_mul_hi_u32_u24_e32 v5, s22, v4
	v_mul_u32_u24_e32 v4, s22, v4
	v_lshl_add_u64 v[126:127], v[4:5], 2, v[2:3]
	v_or_b32_e32 v4, 58, v1
	v_mul_hi_u32_u24_e32 v5, s22, v4
	v_mul_u32_u24_e32 v4, s22, v4
	v_lshl_add_u64 v[128:129], v[4:5], 2, v[2:3]
	v_or_b32_e32 v4, 60, v1
	v_mul_hi_u32_u24_e32 v5, s22, v4
	v_mul_u32_u24_e32 v4, s22, v4
	v_or_b32_e32 v1, 62, v1
	v_lshl_add_u64 v[130:131], v[4:5], 2, v[2:3]
	v_mul_hi_u32_u24_e32 v5, s22, v1
	v_mul_u32_u24_e32 v4, s22, v1
	v_lshl_add_u64 v[132:133], v[4:5], 2, v[2:3]
	global_load_dword v2, v[16:17], off
	global_load_dword v1, v[18:19], off
	global_load_dword v4, v[20:21], off
	global_load_dword v3, v[22:23], off
	global_load_dword v6, v[24:25], off
	global_load_dword v5, v[26:27], off
	global_load_dword v8, v[28:29], off
	global_load_dword v7, v[30:31], off
	global_load_dword v10, v[50:51], off
	global_load_dword v9, v[52:53], off
	global_load_dword v12, v[54:55], off
	global_load_dword v11, v[56:57], off
	global_load_dword v14, v[58:59], off
	global_load_dword v13, v[96:97], off
	global_load_dword v16, v[98:99], off
	global_load_dword v15, v[100:101], off
	global_load_dword v18, v[102:103], off
	global_load_dword v17, v[104:105], off
	global_load_dword v20, v[106:107], off
	global_load_dword v19, v[108:109], off
	global_load_dword v22, v[110:111], off
	global_load_dword v21, v[112:113], off
	global_load_dword v24, v[114:115], off
	global_load_dword v23, v[116:117], off
	global_load_dword v26, v[118:119], off
	global_load_dword v25, v[120:121], off
	global_load_dword v28, v[122:123], off
	global_load_dword v27, v[124:125], off
	global_load_dword v30, v[126:127], off
	global_load_dword v29, v[128:129], off
	global_load_dword v32, v[130:131], off
	global_load_dword v31, v[132:133], off
	s_waitcnt vmcnt(32)
	s_branch .Lmy_cB_s2
; #define LAS __attribute__((address_space(3)))
; __device__ __forceinline__ float clamp_f8(float v) { return __builtin_amdgcn_fmed3f(v, -448.f, 448.f); }
; #define LDS_WAIT() asm volatile("s_waitcnt lgkmcnt(0)" ::: "memory")
; __device__ __forceinline__ void conv_store(const ConvDesc& d, const float (&v)[32], LAS float* scr, int lane) {
; #pragma unroll
;     for (int i = 0; i < 32; ++i) { const int kk = 2 * i + (lane >> 5); scr[kk * 33 + (lane & 31)] = pg8::clamp_f8(v[i] * d.sc); }
;     LDS_WAIT(); asm volatile("" ::: "memory");
;     const int n = lane & 31, h = lane >> 5; const LAS float* sp = scr + (32 * h) * 33 + n;
;     u32x4 o0, o1;
; #pragma unroll
;     for (int q = 0; q < 4; ++q) { int w0 = 0, w1 = 0;
;         w0 = __builtin_amdgcn_cvt_pk_fp8_f32(sp[(4 * q + 0) * 33], sp[(4 * q + 1) * 33], w0, false); w0 = __builtin_amdgcn_cvt_pk_fp8_f32(sp[(4 * q + 2) * 33], sp[(4 * q + 3) * 33], w0, true);
;         w1 = __builtin_amdgcn_cvt_pk_fp8_f32(sp[(16 + 4 * q + 0) * 33], sp[(16 + 4 * q + 1) * 33], w1, false); w1 = __builtin_amdgcn_cvt_pk_fp8_f32(sp[(16 + 4 * q + 2) * 33], sp[(16 + 4 * q + 3) * 33], w1, true);
;         o0[q] = (unsigned)w0; o1[q] = (unsigned)w1; }
;     unsigned char* dp = d.dst + (size_t)n * d.Kd + d.k0 + 32 * h;
;     *(u32x4*)dp = o0; *(u32x4*)(dp + 16) = o1;
;     LDS_WAIT(); asm volatile("" ::: "memory");
.LBB0_969:
	s_waitcnt vmcnt(0)
.Lmy_cB_s2:
	v_mul_f32_e32 v36, s52, v70
	v_mul_f32_e32 v49, s52, v69
	v_med3_f32 v36, v36, s49, v60
	v_med3_f32 v49, v49, s49, v60
	ds_write2_b32 v61, v36, v49 offset1:66
	v_mul_f32_e32 v36, s52, v68
	v_mul_f32_e32 v49, s52, v67
	v_med3_f32 v36, v36, s49, v60
	v_med3_f32 v49, v49, s49, v60
	ds_write2_b32 v61, v36, v49 offset0:132 offset1:198
	v_mul_f32_e32 v36, s52, v66
	v_mul_f32_e32 v49, s52, v65
	v_med3_f32 v36, v36, s49, v60
	v_med3_f32 v49, v49, s49, v60
	ds_write2_b32 v40, v36, v49 offset0:8 offset1:74
	v_mul_f32_e32 v36, s52, v64
	v_mul_f32_e32 v49, s52, v63
	v_med3_f32 v36, v36, s49, v60
	v_med3_f32 v49, v49, s49, v60
	ds_write2_b32 v40, v36, v49 offset0:140 offset1:206
	v_mul_f32_e32 v36, s52, v78
	v_mul_f32_e32 v40, s52, v77
	v_med3_f32 v36, v36, s49, v60
	v_med3_f32 v40, v40, s49, v60
	ds_write2_b32 v41, v36, v40 offset0:16 offset1:82
	v_mul_f32_e32 v36, s52, v76
	v_mul_f32_e32 v40, s52, v75
	v_med3_f32 v36, v36, s49, v60
	v_med3_f32 v40, v40, s49, v60
	ds_write2_b32 v41, v36, v40 offset0:148 offset1:214
	v_mul_f32_e32 v36, s52, v74
	v_mul_f32_e32 v40, s52, v73
	v_med3_f32 v36, v36, s49, v60
	v_med3_f32 v40, v40, s49, v60
	ds_write2_b32 v42, v36, v40 offset0:24 offset1:90
	v_mul_f32_e32 v36, s52, v72
	v_mul_f32_e32 v40, s52, v71
	v_med3_f32 v36, v36, s49, v60
	v_med3_f32 v40, v40, s49, v60
	ds_write2_b32 v42, v36, v40 offset0:156 offset1:222
	v_mul_f32_e32 v36, s52, v86
	v_mul_f32_e32 v40, s52, v85
	v_med3_f32 v36, v36, s49, v60
	v_med3_f32 v40, v40, s49, v60
	ds_write2_b32 v43, v36, v40 offset0:32 offset1:98
	v_mul_f32_e32 v36, s52, v84
	v_mul_f32_e32 v40, s52, v83
	v_med3_f32 v36, v36, s49, v60
	v_med3_f32 v40, v40, s49, v60
	ds_write2_b32 v43, v36, v40 offset0:164 offset1:230
	v_mul_f32_e32 v36, s52, v82
	v_mul_f32_e32 v40, s52, v81
	v_med3_f32 v36, v36, s49, v60
	v_med3_f32 v40, v40, s49, v60
	ds_write2_b32 v44, v36, v40 offset0:40 offset1:106
	v_mul_f32_e32 v36, s52, v80
	v_mul_f32_e32 v40, s52, v79
	v_med3_f32 v36, v36, s49, v60
	v_med3_f32 v40, v40, s49, v60
	ds_write2_b32 v44, v36, v40 offset0:172 offset1:238
	v_mul_f32_e32 v36, s52, v94
	v_mul_f32_e32 v40, s52, v93
	v_med3_f32 v36, v36, s49, v60
	v_med3_f32 v40, v40, s49, v60
	ds_write2_b32 v45, v36, v40 offset0:48 offset1:114
	v_mul_f32_e32 v36, s52, v92
	v_mul_f32_e32 v40, s52, v91
	v_med3_f32 v36, v36, s49, v60
	v_med3_f32 v40, v40, s49, v60
	ds_write2_b32 v45, v36, v40 offset0:180 offset1:246
	v_mul_f32_e32 v36, s52, v90
	v_mul_f32_e32 v40, s52, v89
	v_med3_f32 v36, v36, s49, v60
	v_med3_f32 v40, v40, s49, v60
	ds_write2_b32 v46, v36, v40 offset0:56 offset1:122
	v_mul_f32_e32 v36, s52, v88
	v_mul_f32_e32 v40, s52, v87
	v_med3_f32 v36, v36, s49, v60
	v_med3_f32 v40, v40, s49, v60
	ds_write2_b32 v46, v36, v40 offset0:188 offset1:254
	s_waitcnt lgkmcnt(0)
	ds_read2_b32 v[42:43], v62 offset1:33
	v_mov_b32_e32 v40, v37
	ds_read2_b32 v[44:45], v62 offset0:66 offset1:99
	v_mov_b32_e32 v41, v37
	ds_read2_b32 v[52:53], v48 offset0:148 offset1:181
	s_waitcnt lgkmcnt(2)
	v_cvt_pk_fp8_f32 v40, v42, v43
	ds_read2_b32 v[42:43], v48 offset0:16 offset1:49
	v_mov_b32_e32 v50, v37
	v_mov_b32_e32 v51, v37
	s_waitcnt lgkmcnt(2)
	v_cvt_pk_fp8_f32 v40, v44, v45 op_sel:[0,0,1]
	ds_read2_b32 v[44:45], v62 offset0:132 offset1:165
	s_waitcnt lgkmcnt(1)
	v_cvt_pk_fp8_f32 v50, v42, v43
	ds_read2_b32 v[42:43], v48 offset0:82 offset1:115
	v_cvt_pk_fp8_f32 v51, v52, v53
	ds_read2_b32 v[52:53], v33 offset0:8 offset1:41
	s_waitcnt lgkmcnt(2)
	v_cvt_pk_fp8_f32 v41, v44, v45
	ds_read2_b32 v[44:45], v62 offset0:198 offset1:231
	ds_read2_b32 v[48:49], v48 offset0:214 offset1:247
	ds_read2_b32 v[54:55], v33 offset0:140 offset1:173
	ds_read2_b32 v[56:57], v47 offset0:156 offset1:189
	s_waitcnt lgkmcnt(5)
	v_cvt_pk_fp8_f32 v50, v42, v43 op_sel:[0,0,1]
	s_waitcnt lgkmcnt(3)
	v_cvt_pk_fp8_f32 v41, v44, v45 op_sel:[0,0,1]
	ds_read2_b32 v[44:45], v47 offset0:24 offset1:57
	v_mov_b32_e32 v42, v37
	v_cvt_pk_fp8_f32 v42, v52, v53
	v_mov_b32_e32 v52, v37
	v_mov_b32_e32 v43, v37
	s_waitcnt lgkmcnt(3)
	v_cvt_pk_fp8_f32 v51, v48, v49 op_sel:[0,0,1]
	ds_read2_b32 v[48:49], v33 offset0:74 offset1:107
	s_waitcnt lgkmcnt(1)
	v_cvt_pk_fp8_f32 v52, v44, v45
	ds_read2_b32 v[44:45], v47 offset0:90 offset1:123
	v_cvt_pk_fp8_f32 v43, v54, v55
	ds_read2_b32 v[54:55], v33 offset0:206 offset1:239
	v_mov_b32_e32 v53, v37
	ds_read2_b32 v[46:47], v47 offset0:222 offset1:255
	v_cvt_pk_fp8_f32 v53, v56, v57
	s_waitcnt lgkmcnt(3)
	v_cvt_pk_fp8_f32 v42, v48, v49 op_sel:[0,0,1]
	s_waitcnt lgkmcnt(2)
	v_cvt_pk_fp8_f32 v52, v44, v45 op_sel:[0,0,1]
	s_waitcnt lgkmcnt(1)
	v_cvt_pk_fp8_f32 v43, v54, v55 op_sel:[0,0,1]
	v_mov_b64_e32 v[44:45], s[18:19]
	s_waitcnt lgkmcnt(0)
	v_cvt_pk_fp8_f32 v53, v46, v47 op_sel:[0,0,1]
	v_mad_u64_u32 v[44:45], s[22:23], s51, v34, v[44:45]
	s_mov_b32 s11, s5
	v_lshl_add_u64 v[44:45], v[44:45], 0, s[10:11]
	v_lshl_add_u64 v[44:45], v[44:45], 0, v[38:39]
	global_store_dwordx4 v[44:45], v[40:43], off
	global_store_dwordx4 v[44:45], v[50:53], off offset:16
	s_waitcnt lgkmcnt(0)
	s_add_i32 s46, s46, 0x400000
	s_addk_i32 s47, 0x800
	s_add_i32 s48, s48, 0x10000
	s_addk_i32 s36, 0x1000
	s_cmp_gt_i32 s50, 0x17dff
	s_cselect_b64 s[22:23], -1, 0

; __device__ __forceinline__ ConvDesc expert_desc(Frame& F, int r) {
;     ...
;     else { r -= I_G1; const int e = r >> 9, r2 = r & 511, kb = r2 >> 6, nb = r2 & 63;
;         d.src = (e < NEXP ? INF(I_WED) + (size_t)e * 512 * 2048 : INF(I_WSD)) + nb * 32;
;         d.ldw = 2048; d.k0 = kb * 64; d.dst = WSP(unsigned char, WS_WG2) + ((size_t)e * 2048 + nb * 32) * 512; d.Kd = 512; d.sc = pg8::F8_SW2; }
;     return d;
; }
; __device__ __forceinline__ void conv_load(const ConvDesc& d, float (&v)[32], int lane) {
; #pragma unroll
;     for (int i = 0; i < 32; ++i) { const int kk = 2 * i + (lane >> 5); v[i] = d.src[(size_t)(d.k0 + kk) * d.ldw + (lane & 31)]; }
; }
.LBB0_993:
	v_or_b32_e32 v33, s10, v35
	v_lshlrev_b32_e32 v36, 2, v34
	v_lshl_add_u64 v[40:41], s[38:39], 0, v[36:37]
	v_or_b32_e32 v36, 2, v33
	v_mul_hi_u32_u24_e32 v45, s24, v36
	v_mul_u32_u24_e32 v44, s24, v36
	v_or_b32_e32 v36, 4, v33
	v_mul_hi_u32_u24_e32 v47, s24, v36
	v_mul_u32_u24_e32 v46, s24, v36
	v_or_b32_e32 v36, 6, v33
	v_mul_hi_u32_u24_e32 v49, s24, v36
	v_mul_u32_u24_e32 v48, s24, v36
	v_or_b32_e32 v36, 8, v33
	v_mul_hi_u32_u24_e32 v51, s24, v36
	v_mul_u32_u24_e32 v50, s24, v36
	v_or_b32_e32 v36, 10, v33
	v_mul_hi_u32_u24_e32 v53, s24, v36
	v_mul_u32_u24_e32 v52, s24, v36
	v_or_b32_e32 v36, 12, v33
	v_mul_hi_u32_u24_e32 v43, s24, v33
	v_mul_u32_u24_e32 v42, s24, v33
	v_mul_hi_u32_u24_e32 v55, s24, v36
	v_mul_u32_u24_e32 v54, s24, v36
	v_or_b32_e32 v36, 14, v33
	v_lshl_add_u64 v[42:43], v[42:43], 2, v[40:41]
	v_mul_hi_u32_u24_e32 v57, s24, v36
	v_mul_u32_u24_e32 v56, s24, v36
	v_or_b32_e32 v36, 16, v33
	v_lshl_add_u64 v[44:45], v[44:45], 2, v[40:41]
	v_lshl_add_u64 v[46:47], v[46:47], 2, v[40:41]
	v_lshl_add_u64 v[48:49], v[48:49], 2, v[40:41]
	v_lshl_add_u64 v[50:51], v[50:51], 2, v[40:41]
	v_lshl_add_u64 v[52:53], v[52:53], 2, v[40:41]
	v_lshl_add_u64 v[54:55], v[54:55], 2, v[40:41]
	v_lshl_add_u64 v[56:57], v[56:57], 2, v[40:41]
	global_load_dword v70, v[42:43], off
	global_load_dword v69, v[44:45], off
	global_load_dword v68, v[46:47], off
	global_load_dword v67, v[48:49], off
	global_load_dword v66, v[50:51], off
	global_load_dword v65, v[52:53], off
	global_load_dword v64, v[54:55], off
	global_load_dword v63, v[56:57], off
	v_mul_hi_u32_u24_e32 v43, s24, v36
	v_mul_u32_u24_e32 v42, s24, v36
	v_or_b32_e32 v36, 18, v33
	v_mul_hi_u32_u24_e32 v45, s24, v36
	v_mul_u32_u24_e32 v44, s24, v36
	v_or_b32_e32 v36, 20, v33
	v_mul_hi_u32_u24_e32 v47, s24, v36
	v_mul_u32_u24_e32 v46, s24, v36
	v_or_b32_e32 v36, 22, v33
	v_mul_hi_u32_u24_e32 v49, s24, v36
	v_mul_u32_u24_e32 v48, s24, v36
	v_or_b32_e32 v36, 24, v33
	v_mul_hi_u32_u24_e32 v51, s24, v36
	v_mul_u32_u24_e32 v50, s24, v36
	v_or_b32_e32 v36, 26, v33
	v_mul_hi_u32_u24_e32 v53, s24, v36
	v_mul_u32_u24_e32 v52, s24, v36
	v_or_b32_e32 v36, 28, v33
	v_mul_hi_u32_u24_e32 v55, s24, v36
	v_mul_u32_u24_e32 v54, s24, v36
	v_or_b32_e32 v36, 30, v33
	v_lshl_add_u64 v[42:43], v[42:43], 2, v[40:41]
	v_mul_hi_u32_u24_e32 v57, s24, v36
	v_mul_u32_u24_e32 v56, s24, v36
	v_or_b32_e32 v36, 32, v33
	v_lshl_add_u64 v[44:45], v[44:45], 2, v[40:41]
	v_lshl_add_u64 v[46:47], v[46:47], 2, v[40:41]
	v_lshl_add_u64 v[48:49], v[48:49], 2, v[40:41]
	v_lshl_add_u64 v[50:51], v[50:51], 2, v[40:41]
	v_lshl_add_u64 v[52:53], v[52:53], 2, v[40:41]
	v_lshl_add_u64 v[54:55], v[54:55], 2, v[40:41]
	v_lshl_add_u64 v[56:57], v[56:57], 2, v[40:41]
	global_load_dword v78, v[42:43], off
	global_load_dword v77, v[44:45], off
	global_load_dword v76, v[46:47], off
	global_load_dword v75, v[48:49], off
	global_load_dword v74, v[50:51], off
	global_load_dword v73, v[52:53], off
	global_load_dword v72, v[54:55], off
	global_load_dword v71, v[56:57], off
	v_mul_hi_u32_u24_e32 v43, s24, v36
	v_mul_u32_u24_e32 v42, s24, v36
	v_or_b32_e32 v36, 34, v33
	v_mul_hi_u32_u24_e32 v45, s24, v36
	v_mul_u32_u24_e32 v44, s24, v36
	v_or_b32_e32 v36, 36, v33
	v_mul_hi_u32_u24_e32 v47, s24, v36
	v_mul_u32_u24_e32 v46, s24, v36
	v_or_b32_e32 v36, 38, v33
	v_mul_hi_u32_u24_e32 v49, s24, v36
	v_mul_u32_u24_e32 v48, s24, v36
	v_or_b32_e32 v36, 40, v33
	v_mul_hi_u32_u24_e32 v51, s24, v36
	v_mul_u32_u24_e32 v50, s24, v36
	v_or_b32_e32 v36, 42, v33
	v_mul_hi_u32_u24_e32 v53, s24, v36
	v_mul_u32_u24_e32 v52, s24, v36
	v_or_b32_e32 v36, 44, v33
	v_mul_hi_u32_u24_e32 v55, s24, v36
	v_mul_u32_u24_e32 v54, s24, v36
	v_or_b32_e32 v36, 46, v33
	v_lshl_add_u64 v[42:43], v[42:43], 2, v[40:41]
	v_mul_hi_u32_u24_e32 v57, s24, v36
	v_mul_u32_u24_e32 v56, s24, v36
	v_or_b32_e32 v36, 48, v33
	v_lshl_add_u64 v[44:45], v[44:45], 2, v[40:41]
	v_lshl_add_u64 v[46:47], v[46:47], 2, v[40:41]
	v_lshl_add_u64 v[48:49], v[48:49], 2, v[40:41]
	v_lshl_add_u64 v[50:51], v[50:51], 2, v[40:41]
	v_lshl_add_u64 v[52:53], v[52:53], 2, v[40:41]
	v_lshl_add_u64 v[54:55], v[54:55], 2, v[40:41]
	v_lshl_add_u64 v[56:57], v[56:57], 2, v[40:41]
	global_load_dword v86, v[42:43], off
	global_load_dword v85, v[44:45], off
	global_load_dword v84, v[46:47], off
	global_load_dword v83, v[48:49], off
	global_load_dword v82, v[50:51], off
	global_load_dword v81, v[52:53], off
	global_load_dword v80, v[54:55], off
	global_load_dword v79, v[56:57], off
	v_mul_hi_u32_u24_e32 v43, s24, v36
	v_mul_u32_u24_e32 v42, s24, v36
	v_or_b32_e32 v36, 50, v33
	v_mul_hi_u32_u24_e32 v45, s24, v36
	v_mul_u32_u24_e32 v44, s24, v36
	v_or_b32_e32 v36, 52, v33
	v_mul_hi_u32_u24_e32 v47, s24, v36
	v_mul_u32_u24_e32 v46, s24, v36
	v_or_b32_e32 v36, 54, v33
	v_mul_hi_u32_u24_e32 v49, s24, v36
	v_mul_u32_u24_e32 v48, s24, v36
	v_or_b32_e32 v36, 56, v33
	v_mul_hi_u32_u24_e32 v51, s24, v36
	v_mul_u32_u24_e32 v50, s24, v36
	v_or_b32_e32 v36, 58, v33
	v_mul_hi_u32_u24_e32 v53, s24, v36
	v_mul_u32_u24_e32 v52, s24, v36
	v_or_b32_e32 v36, 60, v33
	v_or_b32_e32 v33, 62, v33
	v_lshl_add_u64 v[42:43], v[42:43], 2, v[40:41]
	v_mul_hi_u32_u24_e32 v55, s24, v36
	v_mul_u32_u24_e32 v54, s24, v36
	v_mul_hi_u32_u24_e32 v57, s24, v33
	v_mul_u32_u24_e32 v56, s24, v33
	v_lshl_add_u64 v[44:45], v[44:45], 2, v[40:41]
	v_lshl_add_u64 v[46:47], v[46:47], 2, v[40:41]
	v_lshl_add_u64 v[48:49], v[48:49], 2, v[40:41]
	v_lshl_add_u64 v[50:51], v[50:51], 2, v[40:41]
	v_lshl_add_u64 v[52:53], v[52:53], 2, v[40:41]
	v_lshl_add_u64 v[54:55], v[54:55], 2, v[40:41]
	v_lshl_add_u64 v[40:41], v[56:57], 2, v[40:41]
	global_load_dword v94, v[42:43], off
	global_load_dword v93, v[44:45], off
	global_load_dword v92, v[46:47], off
	global_load_dword v91, v[48:49], off
	global_load_dword v90, v[50:51], off
	global_load_dword v89, v[52:53], off
	global_load_dword v88, v[54:55], off
	global_load_dword v87, v[40:41], off
	s_branch .LBB0_994

; #define LAS __attribute__((address_space(3)))
; __device__ __forceinline__ float clamp_f8(float v) { return __builtin_amdgcn_fmed3f(v, -448.f, 448.f); }
; #define LDS_WAIT() asm volatile("s_waitcnt lgkmcnt(0)" ::: "memory")
; __device__ __forceinline__ void conv_store(const ConvDesc& d, const float (&v)[32], LAS float* scr, int lane) {
; #pragma unroll
;     for (int i = 0; i < 32; ++i) { const int kk = 2 * i + (lane >> 5); scr[kk * 33 + (lane & 31)] = pg8::clamp_f8(v[i] * d.sc); }
;     LDS_WAIT(); asm volatile("" ::: "memory");
;     const int n = lane & 31, h = lane >> 5; const LAS float* sp = scr + (32 * h) * 33 + n;
;     u32x4 o0, o1;
; #pragma unroll
;     for (int q = 0; q < 4; ++q) { int w0 = 0, w1 = 0;
;         w0 = __builtin_amdgcn_cvt_pk_fp8_f32(sp[(4 * q + 0) * 33], sp[(4 * q + 1) * 33], w0, false); w0 = __builtin_amdgcn_cvt_pk_fp8_f32(sp[(4 * q + 2) * 33], sp[(4 * q + 3) * 33], w0, true);
;         w1 = __builtin_amdgcn_cvt_pk_fp8_f32(sp[(16 + 4 * q + 0) * 33], sp[(16 + 4 * q + 1) * 33], w1, false); w1 = __builtin_amdgcn_cvt_pk_fp8_f32(sp[(16 + 4 * q + 2) * 33], sp[(16 + 4 * q + 3) * 33], w1, true);
;         o0[q] = (unsigned)w0; o1[q] = (unsigned)w1; }
;     unsigned char* dp = d.dst + (size_t)n * d.Kd + d.k0 + 32 * h;
;     *(u32x4*)dp = o0; *(u32x4*)(dp + 16) = o1;
;     LDS_WAIT(); asm volatile("" ::: "memory");
; }
; __device__ __forceinline__ void convert_expert_range(Frame& F, int first, int end, int stride, LAS float* scr) {
;     if (first >= end) return;
;     const int lane = F.lane;
;     float va[32], vb[32];
;     ConvDesc da = expert_desc(F, first), db = da; conv_load(da, va, lane);
;     for (int it = first; ; it += 2 * stride) {
;         const bool h1 = it + stride < end; if (h1) { db = expert_desc(F, it + stride); conv_load(db, vb, lane); }
;         conv_store(da, va, scr, lane);
;         if (!h1) break;
;         const bool h2 = it + 2 * stride < end; if (h2) { da = expert_desc(F, it + 2 * stride); conv_load(da, va, lane); }
;         conv_store(db, vb, scr, lane);
;         if (!h2) break;
;     }
.LBB0_994:
	s_waitcnt vmcnt(63)
	v_mul_f32_e32 v33, s40, v2
	s_waitcnt vmcnt(62)
	v_mul_f32_e32 v36, s40, v1
	v_med3_f32 v33, v33, s49, v60
	v_med3_f32 v36, v36, s49, v60
	ds_write2_b32 v61, v33, v36 offset1:66
	s_waitcnt vmcnt(61)
	v_mul_f32_e32 v33, s40, v4
	s_waitcnt vmcnt(60)
	v_mul_f32_e32 v36, s40, v3
	v_med3_f32 v33, v33, s49, v60
	v_med3_f32 v36, v36, s49, v60
	ds_write2_b32 v61, v33, v36 offset0:132 offset1:198
	s_waitcnt vmcnt(59)
	v_mul_f32_e32 v33, s40, v6
	s_waitcnt vmcnt(58)
	v_mul_f32_e32 v36, s40, v5
	v_med3_f32 v33, v33, s49, v60
	v_med3_f32 v36, v36, s49, v60
	v_add_u32_e32 v40, 0x400, v61
	ds_write2_b32 v40, v33, v36 offset0:8 offset1:74
	s_waitcnt vmcnt(57)
	v_mul_f32_e32 v33, s40, v8
	s_waitcnt vmcnt(56)
	v_mul_f32_e32 v36, s40, v7
	v_med3_f32 v33, v33, s49, v60
	v_med3_f32 v36, v36, s49, v60
	ds_write2_b32 v40, v33, v36 offset0:140 offset1:206
	s_waitcnt vmcnt(55)
	v_mul_f32_e32 v33, s40, v10
	s_waitcnt vmcnt(54)
	v_mul_f32_e32 v36, s40, v9
	v_med3_f32 v33, v33, s49, v60
	v_med3_f32 v36, v36, s49, v60
	v_add_u32_e32 v41, 0x800, v61
	ds_write2_b32 v41, v33, v36 offset0:16 offset1:82
	s_waitcnt vmcnt(53)
	v_mul_f32_e32 v33, s40, v12
	s_waitcnt vmcnt(52)
	v_mul_f32_e32 v36, s40, v11
	v_med3_f32 v33, v33, s49, v60
	v_med3_f32 v36, v36, s49, v60
	ds_write2_b32 v41, v33, v36 offset0:148 offset1:214
	s_waitcnt vmcnt(51)
	v_mul_f32_e32 v33, s40, v14
	s_waitcnt vmcnt(50)
	v_mul_f32_e32 v36, s40, v13
	v_med3_f32 v33, v33, s49, v60
	v_med3_f32 v36, v36, s49, v60
	v_add_u32_e32 v42, 0xc00, v61
	ds_write2_b32 v42, v33, v36 offset0:24 offset1:90
	s_waitcnt vmcnt(49)
	v_mul_f32_e32 v33, s40, v16
	s_waitcnt vmcnt(48)
	v_mul_f32_e32 v36, s40, v15
	v_med3_f32 v33, v33, s49, v60
	v_med3_f32 v36, v36, s49, v60
	ds_write2_b32 v42, v33, v36 offset0:156 offset1:222
	s_waitcnt vmcnt(47)
	v_mul_f32_e32 v33, s40, v18
	s_waitcnt vmcnt(46)
	v_mul_f32_e32 v36, s40, v17
	v_med3_f32 v33, v33, s49, v60
	v_med3_f32 v36, v36, s49, v60
	v_add_u32_e32 v43, 0x1000, v61
	ds_write2_b32 v43, v33, v36 offset0:32 offset1:98
	s_waitcnt vmcnt(45)
	v_mul_f32_e32 v33, s40, v20
	s_waitcnt vmcnt(44)
	v_mul_f32_e32 v36, s40, v19
	v_med3_f32 v33, v33, s49, v60
	v_med3_f32 v36, v36, s49, v60
	ds_write2_b32 v43, v33, v36 offset0:164 offset1:230
	s_waitcnt vmcnt(43)
	v_mul_f32_e32 v33, s40, v22
	s_waitcnt vmcnt(42)
	v_mul_f32_e32 v36, s40, v21
	v_med3_f32 v33, v33, s49, v60
	v_med3_f32 v36, v36, s49, v60
	v_add_u32_e32 v44, 0x1400, v61
	ds_write2_b32 v44, v33, v36 offset0:40 offset1:106
	s_waitcnt vmcnt(41)
	v_mul_f32_e32 v33, s40, v24
	s_waitcnt vmcnt(40)
	v_mul_f32_e32 v36, s40, v23
	v_med3_f32 v33, v33, s49, v60
	v_med3_f32 v36, v36, s49, v60
	ds_write2_b32 v44, v33, v36 offset0:172 offset1:238
	s_waitcnt vmcnt(39)
	v_mul_f32_e32 v33, s40, v26
	s_waitcnt vmcnt(38)
	v_mul_f32_e32 v36, s40, v25
	v_med3_f32 v33, v33, s49, v60
	v_med3_f32 v36, v36, s49, v60
	v_add_u32_e32 v45, 0x1800, v61
	ds_write2_b32 v45, v33, v36 offset0:48 offset1:114
	s_waitcnt vmcnt(37)
	v_mul_f32_e32 v33, s40, v28
	s_waitcnt vmcnt(36)
	v_mul_f32_e32 v36, s40, v27
	v_med3_f32 v33, v33, s49, v60
	v_med3_f32 v36, v36, s49, v60
	ds_write2_b32 v45, v33, v36 offset0:180 offset1:246
	s_waitcnt vmcnt(35)
	v_mul_f32_e32 v33, s40, v30
	s_waitcnt vmcnt(34)
	v_mul_f32_e32 v36, s40, v29
	v_med3_f32 v33, v33, s49, v60
	v_med3_f32 v36, v36, s49, v60
	v_add_u32_e32 v46, 0x1c00, v61
	ds_write2_b32 v46, v33, v36 offset0:56 offset1:122
	s_waitcnt vmcnt(33)
	v_mul_f32_e32 v33, s40, v32
	s_waitcnt vmcnt(32)
	v_mul_f32_e32 v36, s40, v31
	v_med3_f32 v33, v33, s49, v60
	v_med3_f32 v36, v36, s49, v60
	ds_write2_b32 v46, v33, v36 offset0:188 offset1:254
	s_waitcnt lgkmcnt(0)
	ds_read2_b32 v[50:51], v62 offset1:33
	v_mov_b32_e32 v48, 0
	v_mov_b32_e32 v49, 0
	v_add_u32_e32 v33, 0x400, v62
	ds_read2_b32 v[52:53], v33 offset0:8 offset1:41
	s_waitcnt lgkmcnt(1)
	v_cvt_pk_fp8_f32 v48, v50, v51
	ds_read2_b32 v[50:51], v62 offset0:66 offset1:99
	s_mov_b32 s7, s5
	v_add_u32_e32 v47, 0xc00, v62
	ds_read2_b32 v[56:57], v47 offset0:24 offset1:57
	s_andn2_b64 vcc, exec, s[22:23]
	s_waitcnt lgkmcnt(1)
	v_cvt_pk_fp8_f32 v48, v50, v51 op_sel:[0,0,1]
	ds_read2_b32 v[50:51], v62 offset0:132 offset1:165
	s_mov_b64 s[22:23], -1
	s_waitcnt lgkmcnt(0)
	v_cvt_pk_fp8_f32 v49, v50, v51
	ds_read2_b32 v[50:51], v62 offset0:198 offset1:231
	s_waitcnt lgkmcnt(0)
	v_cvt_pk_fp8_f32 v49, v50, v51 op_sel:[0,0,1]
	v_mov_b32_e32 v50, 0
	v_cvt_pk_fp8_f32 v50, v52, v53
	ds_read2_b32 v[52:53], v33 offset0:74 offset1:107
	v_mov_b32_e32 v51, 0
	s_waitcnt lgkmcnt(0)
	v_cvt_pk_fp8_f32 v50, v52, v53 op_sel:[0,0,1]
	ds_read2_b32 v[52:53], v33 offset0:140 offset1:173
	s_waitcnt lgkmcnt(0)
	v_cvt_pk_fp8_f32 v51, v52, v53
	ds_read2_b32 v[52:53], v33 offset0:206 offset1:239
	s_waitcnt lgkmcnt(0)
	v_cvt_pk_fp8_f32 v51, v52, v53 op_sel:[0,0,1]
	v_mov_b64_e32 v[52:53], s[8:9]
	v_mad_u64_u32 v[52:53], s[24:25], s37, v34, v[52:53]
	v_lshl_add_u64 v[52:53], v[52:53], 0, s[6:7]
	v_lshl_add_u64 v[54:55], v[52:53], 0, v[38:39]
	global_store_dwordx4 v[54:55], v[48:51], off
	s_nop 1
	v_add_u32_e32 v48, 0x800, v62
	ds_read2_b32 v[52:53], v48 offset0:16 offset1:49
	v_mov_b32_e32 v50, 0
	v_mov_b32_e32 v51, 0
	s_waitcnt lgkmcnt(0)
	v_cvt_pk_fp8_f32 v50, v52, v53
	ds_read2_b32 v[52:53], v48 offset0:82 offset1:115
	s_waitcnt lgkmcnt(0)
	v_cvt_pk_fp8_f32 v50, v52, v53 op_sel:[0,0,1]
	ds_read2_b32 v[52:53], v48 offset0:148 offset1:181
	s_waitcnt lgkmcnt(0)
	v_cvt_pk_fp8_f32 v51, v52, v53
	ds_read2_b32 v[52:53], v48 offset0:214 offset1:247
	s_waitcnt lgkmcnt(0)
	v_cvt_pk_fp8_f32 v51, v52, v53 op_sel:[0,0,1]
	v_mov_b32_e32 v52, 0
	v_cvt_pk_fp8_f32 v52, v56, v57
	ds_read2_b32 v[56:57], v47 offset0:90 offset1:123
	v_mov_b32_e32 v53, 0
	s_waitcnt lgkmcnt(0)
	v_cvt_pk_fp8_f32 v52, v56, v57 op_sel:[0,0,1]
	ds_read2_b32 v[56:57], v47 offset0:156 offset1:189
	s_waitcnt lgkmcnt(0)
	v_cvt_pk_fp8_f32 v53, v56, v57
	ds_read2_b32 v[56:57], v47 offset0:222 offset1:255
	s_waitcnt lgkmcnt(0)
	v_cvt_pk_fp8_f32 v53, v56, v57 op_sel:[0,0,1]
	global_store_dwordx4 v[54:55], v[50:53], off offset:16
	s_waitcnt lgkmcnt(0)
	s_cbranch_vccnz .LBB0_970
	s_cmp_gt_i32 s50, 0x17dff
	s_cbranch_scc1 .LBB0_969
	s_cmp_gt_i32 s50, 0xfbff
	s_cbranch_scc0 .LBB0_1002
	s_add_i32 s4, s47, 0xfffefc00
	s_cmpk_gt_u32 s4, 0x7fff
	s_mov_b64 s[6:7], -1
	s_cbranch_scc0 .LBB0_999
	s_load_dwordx2 s[8:9], s[16:17], 0xb0
	s_mov_b64 s[6:7], 0
